# speedup vs baseline: 1.0147x; 1.0147x over previous
.LBB1_15:
	s_or_b64 exec, exec, s[12:13]
	v_and_b32_e32 v114, 31, v0
	s_mul_i32 s9, s67, 0x60
	s_cmp_lg_u32 s67, 0
	s_cselect_b64 s[74:75], -1, 0
	v_alignbit_b32 v126, v113, v112, 24
	v_cndmask_b32_e64 v126, v112, v126, s[74:75]
	v_bfe_u32 v91, v126, 0, 8
	v_mul_lo_u16_e32 v15, 0x4f, v91
	s_lshl_b32 s7, s66, 3
	v_lshrrev_b16_e32 v15, 9, v15
	s_or_b32 s8, s7, 0xb600
	v_and_b32_e32 v15, 62, v15
	v_add_u32_e32 v15, v91, v15
	s_movk_i32 s6, 0x48
	v_mov_b32_e32 v99, s8
	v_mad_u32_u24 v42, v15, s6, v99
	v_mad_u32_u24 v43, v115, s6, v42
	s_waitcnt lgkmcnt(0)
	s_barrier
	ds_read_b64 v[34:35], v43
	ds_read_b64 v[36:37], v43 offset:8
	ds_read_b64 v[38:39], v43 offset:1080
	ds_read_b64 v[40:41], v43 offset:1088
	v_mov_b32_e32 v2, v46
	v_mov_b32_e32 v3, v46
	v_mov_b32_e32 v4, v46
	v_mov_b32_e32 v5, v46
	v_mov_b32_e32 v6, v47
	v_mov_b32_e32 v7, v47
	v_mov_b32_e32 v8, v47
	v_mov_b32_e32 v9, v47
	v_mov_b32_e32 v10, v48
	v_mov_b32_e32 v11, v48
	v_mov_b32_e32 v12, v48
	v_mov_b32_e32 v13, v48
	v_mov_b32_e32 v14, v49
	v_mov_b32_e32 v15, v49
	v_mov_b32_e32 v16, v49
	v_mov_b32_e32 v17, v49
	s_movk_i32 s8, 0x438
	s_add_i32 s12, s9, 32
	s_waitcnt lgkmcnt(2)
	v_mfma_f32_32x32x16_f16 v[18:33], v[86:89], v[34:37], v[2:17]
	v_add_u32_e32 v34, 0x8b8, v43
	ds_read_b64 v[36:37], v34 offset:8
	ds_read_b64 v[34:35], v34
	v_and_or_b32 v107, v0, 32, s7
	s_movk_i32 s7, 0x110
	v_mad_u32_u24 v91, v91, s7, v107
	s_add_i32 s9, s9, 64
	s_lshr_b32 s42, s3, 6
	s_waitcnt lgkmcnt(2)
	v_mfma_f32_32x32x16_f16 v[18:33], v[62:65], v[38:41], v[18:33]
	v_mad_u32_u24 v38, v115, s8, v42
	ds_read_b64 v[40:41], v38 offset:152
	ds_read_b64 v[38:39], v38 offset:144
	s_cmpk_lt_u32 s3, 0x100
	s_cselect_b64 s[30:31], -1, 0
	s_add_i32 s13, s69, 0x600
	s_add_i32 s14, s69, 0x700
	v_lshlrev_b32_e32 v116, 4, v115
	s_waitcnt lgkmcnt(2)
	v_mfma_f32_32x32x16_f16 v[18:33], v[58:61], v[34:37], v[18:33]
	v_add_u32_e32 v34, 0x870, v43
	ds_read_b64 v[36:37], v34 offset:8
	ds_read_b64 v[34:35], v34
	s_movk_i32 s15, 0x1070
	s_movk_i32 s16, 0x1ba0
	s_movk_i32 s17, 0x1c20
	s_waitcnt lgkmcnt(2)
	v_mfma_f32_32x32x16_f16 v[18:33], v[54:57], v[38:41], v[18:33]
	v_bfe_u32 v101, v126, 8, 8
	v_mul_lo_u16_e32 v38, 0x4f, v101
	v_lshrrev_b16_e32 v38, 9, v38
	v_and_b32_e32 v38, 62, v38
	v_add_u32_e32 v38, v101, v38
	v_mad_u32_u24 v97, v38, s6, v99
	v_mad_u32_u24 v106, v115, s6, v97
	ds_read_b64 v[92:93], v106
	ds_read_b64 v[94:95], v106 offset:8
	v_add_u32_e32 v96, 0x8b8, v106
	ds_read_b64 v[102:103], v96
	ds_read_b64 v[104:105], v96 offset:8
	s_waitcnt lgkmcnt(4)
	v_mfma_f32_32x32x16_f16 v[18:33], v[50:53], v[34:37], v[18:33]
	s_add_i32 s12, s69, 0x500
	s_addk_i32 s69, 0x800
	s_cmpk_gt_u32 s3, 0xff
	s_cselect_b64 vcc, -1, 0
	s_waitcnt lgkmcnt(2)
	v_mfma_f32_32x32x16_f16 v[34:49], v[86:89], v[92:95], v[2:17]
	ds_read_b64 v[92:93], v106 offset:1080
	ds_read_b64 v[94:95], v106 offset:1088
	s_nop 4
	v_cvt_pk_f16_f32 v18, v18, v19
	v_pk_max_f16 v96, v18, 0
	v_mad_u32_u24 v18, v115, s8, v97
	v_cvt_pk_f16_f32 v22, v22, v23
	v_add_u32_e32 v23, 0x870, v106
	v_cvt_pk_f16_f32 v30, v30, v31
	s_waitcnt lgkmcnt(0)
	v_mfma_f32_32x32x16_f16 v[34:49], v[62:65], v[92:95], v[34:49]
	v_cvt_pk_f16_f32 v92, v20, v21
	ds_read_b64 v[20:21], v18 offset:152
	ds_read_b64 v[18:19], v18 offset:144
	v_pk_max_f16 v97, v92, 0
	ds_read_b64 v[92:93], v23
	ds_read_b64 v[94:95], v23 offset:8
	v_cvt_pk_f16_f32 v31, v32, v33
	v_mfma_f32_32x32x16_f16 v[34:49], v[58:61], v[102:105], v[34:49]
	v_or_b32_e32 v102, 64, v114
	s_waitcnt lgkmcnt(2)
	v_mfma_f32_32x32x16_f16 v[34:49], v[54:57], v[18:21], v[34:49]
	v_cvt_pk_f16_f32 v19, v24, v25
	v_pk_max_f16 v18, v22, 0
	v_pk_max_f16 v19, v19, 0
	ds_write2_b64 v91, v[96:97], v[18:19] offset1:8
	v_cvt_pk_f16_f32 v18, v26, v27
	v_pk_max_f16 v26, v18, 0
	v_cvt_pk_f16_f32 v22, v28, v29
	v_bfe_u32 v28, v126, 16, 8
	v_mul_lo_u16_e32 v18, 0x4f, v28
	v_lshrrev_b16_e32 v18, 9, v18
	v_and_b32_e32 v18, 62, v18
	v_add_u32_e32 v18, v28, v18
	v_mad_u32_u24 v29, v18, s6, v99
	s_waitcnt lgkmcnt(1)
	v_mfma_f32_32x32x16_f16 v[34:49], v[50:53], v[92:95], v[34:49]
	v_add_u32_e32 v94, s68, v100
	v_add_u32_e32 v94, s69, v94
	v_mov_b32_e32 v95, 0
	v_lshl_add_u64 v[94:95], v[94:95], 4, s[22:23]
	global_load_dwordx4 v[94:97], v[94:95], off
	v_mad_u32_u24 v92, v115, s6, v29
	ds_read_b64 v[18:19], v92
	ds_read_b64 v[20:21], v92 offset:8
	v_pk_max_f16 v27, v22, 0
	ds_read_b64 v[22:23], v92 offset:1080
	ds_read_b64 v[24:25], v92 offset:1088
	v_or_b32_e32 v99, 32, v114
	s_nop 6
	v_cvt_pk_f16_f32 v32, v40, v41
	s_waitcnt lgkmcnt(2)
	v_mfma_f32_32x32x16_f16 v[2:17], v[86:89], v[18:21], v[2:17]
	v_pk_max_f16 v18, v30, 0
	v_pk_max_f16 v19, v31, 0
	ds_write2_b64 v91, v[26:27], v[18:19] offset0:16 offset1:24
	v_cvt_pk_f16_f32 v18, v34, v35
	v_cvt_pk_f16_f32 v19, v36, v37
	v_pk_max_f16 v26, v18, 0
	v_add_u32_e32 v18, 0x8b8, v92
	s_waitcnt lgkmcnt(1)
	v_mfma_f32_32x32x16_f16 v[2:17], v[62:65], v[22:25], v[2:17]
	v_pk_max_f16 v27, v19, 0
	ds_read_b64 v[20:21], v18 offset:8
	ds_read_b64 v[18:19], v18
	v_mad_u32_u24 v22, v115, s8, v29
	ds_read_b64 v[24:25], v22 offset:152
	ds_read_b64 v[22:23], v22 offset:144
	v_cvt_pk_f16_f32 v31, v38, v39
	v_mad_u32_u24 v30, v101, s7, v107
	s_and_b64 s[8:9], vcc, exec
	s_waitcnt lgkmcnt(2)
	v_mfma_f32_32x32x16_f16 v[2:17], v[58:61], v[18:21], v[2:17]
	v_pk_max_f16 v18, v31, 0
	v_pk_max_f16 v19, v32, 0
	ds_write2_b64 v30, v[26:27], v[18:19] offset1:8
	v_cvt_pk_f16_f32 v18, v42, v43
	v_cvt_pk_f16_f32 v19, v44, v45
	v_pk_max_f16 v26, v18, 0
	v_add_u32_e32 v18, 0x870, v92
	s_waitcnt lgkmcnt(1)
	v_mfma_f32_32x32x16_f16 v[2:17], v[54:57], v[22:25], v[2:17]
	v_pk_max_f16 v27, v19, 0
	ds_read_b64 v[20:21], v18 offset:8
	ds_read_b64 v[18:19], v18
	v_cvt_pk_f16_f32 v22, v46, v47
	v_cvt_pk_f16_f32 v23, v48, v49
	v_pk_max_f16 v22, v22, 0
	v_pk_max_f16 v23, v23, 0
	ds_write2_b64 v30, v[26:27], v[22:23] offset0:16 offset1:24
	s_waitcnt lgkmcnt(1)
	v_mfma_f32_32x32x16_f16 v[2:17], v[50:53], v[18:21], v[2:17]
	v_mad_u32_u24 v18, v28, s7, v107
	v_lshl_or_b32 v42, s66, 5, v116
	s_cselect_b32 s8, 0xf60, 0
	s_movk_i32 s9, 0xff0
	s_cselect_b32 s9, s9, 0x80
	s_cselect_b32 s15, s15, 0x110
	s_cselect_b32 s16, s16, 0x190
	s_nop 4
	v_cvt_pk_f16_f32 v2, v2, v3
	v_cvt_pk_f16_f32 v3, v4, v5
	v_cvt_pk_f16_f32 v4, v6, v7
	v_cvt_pk_f16_f32 v5, v8, v9
	v_pk_max_f16 v2, v2, 0
	v_pk_max_f16 v3, v3, 0
	v_pk_max_f16 v4, v4, 0
	v_pk_max_f16 v5, v5, 0
	ds_write2_b64 v18, v[2:3], v[4:5] offset1:8
	v_cvt_pk_f16_f32 v2, v10, v11
	v_cvt_pk_f16_f32 v3, v12, v13
	v_cvt_pk_f16_f32 v4, v14, v15
	v_cvt_pk_f16_f32 v5, v16, v17
	v_pk_max_f16 v2, v2, 0
	v_pk_max_f16 v3, v3, 0
	v_pk_max_f16 v4, v4, 0
	v_pk_max_f16 v5, v5, 0
	ds_write2_b64 v18, v[2:3], v[4:5] offset0:16 offset1:24
	s_waitcnt vmcnt(0)
	v_bfe_u32 v2, v117, 0, 8
	v_mul_u32_u24_e32 v3, 0xbb, v2
	v_lshrrev_b32_e32 v3, 11, v3
	v_lshl_add_u32 v103, v3, 1, v2
	v_bfe_u32 v2, v117, 8, 8
	v_mul_u32_u24_e32 v3, 0xbb, v2
	v_lshrrev_b32_e32 v3, 11, v3
	v_lshl_add_u32 v106, v3, 1, v2
	v_mad_u32_u24 v90, v103, s7, v42
	v_mad_u32_u24 v91, v106, s7, v42
	v_add_u32_e32 v2, s8, v90
	v_add_u32_e32 v6, s8, v91
	s_waitcnt lgkmcnt(0)
	s_barrier
	ds_read_b128 v[2:5], v2
	ds_read_b128 v[6:9], v6
	s_waitcnt lgkmcnt(1)
	v_mfma_f32_32x32x16_f16 v[18:33], v[82:85], v[2:5], 0
	v_add_u32_e32 v34, s9, v90
	v_add_u32_e32 v38, s9, v91
	ds_read_b128 v[34:37], v34
	ds_read_b128 v[38:41], v38
	s_cselect_b32 s17, s17, 0x220
	v_or_b32_e32 v101, 0x60, v114
	s_waitcnt lgkmcnt(2)
	v_mfma_f32_32x32x16_f16 v[2:17], v[82:85], v[6:9], 0
	s_waitcnt lgkmcnt(1)
	v_mfma_f32_32x32x16_f16 v[18:33], v[74:77], v[34:37], v[18:33]
	v_add_u32_e32 v34, s15, v90
	ds_read_b128 v[34:37], v34
	s_waitcnt lgkmcnt(1)
	v_mfma_f32_32x32x16_f16 v[2:17], v[74:77], v[38:41], v[2:17]
	v_add_u32_e32 v38, s15, v91
	ds_read_b128 v[38:41], v38
	s_waitcnt lgkmcnt(1)
	v_mfma_f32_32x32x16_f16 v[18:33], v[78:81], v[34:37], v[18:33]
	v_add_u32_e32 v34, s16, v90
	ds_read_b128 v[34:37], v34
	s_waitcnt lgkmcnt(1)
	v_mfma_f32_32x32x16_f16 v[2:17], v[78:81], v[38:41], v[2:17]
	v_add_u32_e32 v38, s16, v91
	ds_read_b128 v[38:41], v38
	s_waitcnt lgkmcnt(1)
	v_mfma_f32_32x32x16_f16 v[18:33], v[70:73], v[34:37], v[18:33]
	v_bfe_u32 v43, v117, 16, 8
	v_mul_u32_u24_e32 v34, 0xbb, v43
	v_lshrrev_b32_e32 v104, 11, v34
	v_add_u32_e32 v34, s17, v90
	ds_read_b128 v[34:37], v34
	v_lshl_add_u32 v104, v104, 1, v43
	v_mad_u32_u24 v92, v104, s7, v42
	s_waitcnt lgkmcnt(1)
	v_mfma_f32_32x32x16_f16 v[2:17], v[70:73], v[38:41], v[2:17]
	v_add_u32_e32 v38, s17, v91
	ds_read_b128 v[38:41], v38
	s_waitcnt lgkmcnt(1)
	v_mfma_f32_32x32x16_f16 v[18:33], v[66:69], v[34:37], v[18:33]
	v_bfe_u32 v34, v117, 24, 8
	v_mul_u32_u24_e32 v35, 0xbb, v34
	v_lshrrev_b32_e32 v35, 11, v35
	v_lshl_add_u32 v105, v35, 1, v34
	v_mad_u32_u24 v93, v105, s7, v42
	s_waitcnt lgkmcnt(0)
	v_mfma_f32_32x32x16_f16 v[2:17], v[66:69], v[38:41], v[2:17]
	v_add_u32_e32 v34, s8, v92
	v_add_u32_e32 v38, s8, v93
	ds_read_b128 v[34:37], v34
	ds_read_b128 v[38:41], v38
	v_add_u32_e32 v86, s9, v93
	s_waitcnt lgkmcnt(1)
	v_mfma_f32_32x32x16_f16 v[50:65], v[82:85], v[34:37], 0
	ds_read_b128 v[86:89], v86
	s_waitcnt lgkmcnt(1)
	v_mfma_f32_32x32x16_f16 v[34:49], v[82:85], v[38:41], 0
	v_add_u32_e32 v82, s9, v92
	ds_read_b128 v[82:85], v82
	s_waitcnt lgkmcnt(0)
	v_mfma_f32_32x32x16_f16 v[50:65], v[74:77], v[82:85], v[50:65]
	v_add_u32_e32 v82, s15, v93
	ds_read_b128 v[82:85], v82
	v_mfma_f32_32x32x16_f16 v[34:49], v[74:77], v[86:89], v[34:49]
	v_add_u32_e32 v74, s15, v92
	ds_read_b128 v[74:77], v74
	s_waitcnt lgkmcnt(0)
	v_mfma_f32_32x32x16_f16 v[50:65], v[78:81], v[74:77], v[50:65]
	v_add_u32_e32 v74, s16, v92
	ds_read_b128 v[74:77], v74
	v_mfma_f32_32x32x16_f16 v[34:49], v[78:81], v[82:85], v[34:49]
	v_add_u32_e32 v78, s16, v93
	ds_read_b128 v[78:81], v78
	s_waitcnt lgkmcnt(1)
	v_mfma_f32_32x32x16_f16 v[50:65], v[70:73], v[74:77], v[50:65]
	v_add_u32_e32 v74, s17, v93
	ds_read_b128 v[74:77], v74
	s_waitcnt lgkmcnt(1)
	v_mfma_f32_32x32x16_f16 v[34:49], v[70:73], v[78:81], v[34:49]
	v_add_u32_e32 v70, s17, v92
	ds_read_b128 v[70:73], v70
	s_waitcnt lgkmcnt(0)
	v_mfma_f32_32x32x16_f16 v[50:65], v[66:69], v[70:73], v[50:65]
	v_mfma_f32_32x32x16_f16 v[34:49], v[66:69], v[74:77], v[34:49]
	s_movk_i32 s7, 0x1cb0
	s_cselect_b32 s7, s7, 0x2a0
	v_add_u32_e32 v74, s7, v90
	ds_read_b128 v[74:77], v74
	v_add_u32_e32 v78, s7, v91
	ds_read_b128 v[78:81], v78
	s_movk_i32 s12, 0x1d30
	s_cselect_b32 s12, s12, 0xdd0
	s_movk_i32 s8, 0x1dc0
	s_cselect_b32 s8, s8, 0xe50
	s_movk_i32 s9, 0x1e40
	s_cselect_b32 s9, s9, 0xee0
	s_waitcnt vmcnt(0) lgkmcnt(1)
	v_mfma_f32_32x32x16_f16 v[18:33], v[108:111], v[74:77], v[18:33]
	v_add_u32_e32 v82, s12, v91
	ds_read_b128 v[82:85], v82
	s_waitcnt lgkmcnt(1)
	v_mfma_f32_32x32x16_f16 v[2:17], v[108:111], v[78:81], v[2:17]
	v_add_u32_e32 v78, s12, v90
	ds_read_b128 v[78:81], v78
	s_waitcnt lgkmcnt(0)
	v_mfma_f32_32x32x16_f16 v[18:33], v[118:121], v[78:81], v[18:33]
	v_add_u32_e32 v86, s8, v91
	ds_read_b128 v[86:89], v86
	v_mfma_f32_32x32x16_f16 v[2:17], v[118:121], v[82:85], v[2:17]
	v_add_u32_e32 v82, s8, v90
	ds_read_b128 v[82:85], v82
	s_waitcnt lgkmcnt(0)
	v_mfma_f32_32x32x16_f16 v[18:33], v[122:125], v[82:85], v[18:33]
	v_add_u32_e32 v82, s9, v90
	ds_read_b128 v[82:85], v82
	v_mfma_f32_32x32x16_f16 v[2:17], v[122:125], v[86:89], v[2:17]
	v_add_u32_e32 v86, s9, v91
	ds_read_b128 v[86:89], v86
	s_waitcnt lgkmcnt(1)
	v_mfma_f32_32x32x16_f16 v[18:33], v[94:97], v[82:85], v[18:33]
	s_waitcnt lgkmcnt(0)
	v_mfma_f32_32x32x16_f16 v[2:17], v[94:97], v[86:89], v[2:17]
	v_add_u32_e32 v82, s7, v92
	v_add_u32_e32 v86, s7, v93
	ds_read_b128 v[82:85], v82
	ds_read_b128 v[86:89], v86
	s_waitcnt lgkmcnt(1)
	v_mfma_f32_32x32x16_f16 v[50:65], v[108:111], v[82:85], v[50:65]
	v_add_u32_e32 v82, s12, v93
	ds_read_b128 v[82:85], v82
	s_waitcnt lgkmcnt(1)
	v_mfma_f32_32x32x16_f16 v[34:49], v[108:111], v[86:89], v[34:49]
	v_add_u32_e32 v66, s12, v92
	ds_read_b128 v[66:69], v66
	s_waitcnt lgkmcnt(0)
	v_mfma_f32_32x32x16_f16 v[50:65], v[118:121], v[66:69], v[50:65]
	v_add_u32_e32 v66, s8, v92
	ds_read_b128 v[66:69], v66
	v_mfma_f32_32x32x16_f16 v[34:49], v[118:121], v[82:85], v[34:49]
	v_add_u32_e32 v70, s8, v93
	ds_read_b128 v[70:73], v70
	s_waitcnt lgkmcnt(1)
	v_mfma_f32_32x32x16_f16 v[50:65], v[122:125], v[66:69], v[50:65]
	v_add_u32_e32 v66, s9, v92
	ds_read_b128 v[66:69], v66
	s_waitcnt lgkmcnt(1)
	v_mfma_f32_32x32x16_f16 v[34:49], v[122:125], v[70:73], v[34:49]
	v_add_u32_e32 v70, s9, v93
	ds_read_b128 v[70:73], v70
	s_waitcnt lgkmcnt(1)
	v_mfma_f32_32x32x16_f16 v[50:65], v[94:97], v[66:69], v[50:65]
	s_waitcnt lgkmcnt(0)
	v_mfma_f32_32x32x16_f16 v[34:49], v[94:97], v[70:73], v[34:49]
	s_cmpk_gt_u32 s3, 0x17f
	s_barrier
	s_cbranch_scc1 .LBB1_17
	s_mul_hi_u32 s7, s42, 0x55555556
	s_mul_i32 s7, s7, 3
	s_sub_i32 s7, s42, s7
	s_lshl_b32 s7, s7, 3
	s_add_i32 s8, s7, 0xb600
	s_cmpk_gt_u32 s3, 0xbf
	s_cselect_b64 s[74:75], -1, 0
	s_movk_i32 s12, 0x438
	s_movk_i32 s13, 0xd0
	v_alignbit_b32 v99, v113, v112, 24
	v_cndmask_b32_e64 v99, v112, v99, s[74:75]
	v_add_u32_e32 v122, 0xf550, v98
	ds_read_b128 v[82:85], v98 offset:62800
	ds_read_b128 v[86:89], v98 offset:63824
	ds_read_b128 v[90:93], v98 offset:64848
	ds_read_b128 v[94:97], v122 offset:3072
	ds_read_b128 v[118:121], v122 offset:4096
	ds_read_b32 v107, v122 offset:5120
	ds_read_b32 v112, v122 offset:5124
	ds_read_b32 v113, v122 offset:5128
	ds_read_b32 v117, v122 offset:5132
	v_bfe_u32 v101, v99, 0, 8
	v_mul_lo_u16_e32 v102, 0x4f, v101
	v_lshrrev_b16_e32 v102, 9, v102
	v_and_b32_e32 v102, 62, v102
	v_add_u32_e32 v102, v101, v102
	v_mov_b32_e32 v123, s8
	v_mad_u32_u24 v102, v102, s6, v123
	v_mad_u32_u24 v123, v115, s6, v102
	v_mad_u32_u24 v102, v115, s12, v102
	v_mad_u32_u24 v122, v115, 24, s7
	v_mad_u32_u24 v101, v101, s13, v122
	ds_read_b64 v[108:109], v123 offset:32
	ds_read_b64 v[110:111], v123 offset:40
	ds_read_b64 v[124:125], v123 offset:1112
	ds_read_b64 v[126:127], v123 offset:1120
	s_waitcnt lgkmcnt(2)
	v_mfma_f32_32x32x16_f16 v[66:81], v[82:85], v[108:111], 0
	ds_read_b64 v[108:109], v123 offset:2264
	ds_read_b64 v[110:111], v123 offset:2272
	s_waitcnt lgkmcnt(2)
	v_mfma_f32_32x32x16_f16 v[66:81], v[86:89], v[124:127], v[66:81]
	ds_read_b64 v[124:125], v102 offset:176
	ds_read_b64 v[126:127], v102 offset:184
	s_waitcnt lgkmcnt(2)
	v_mfma_f32_32x32x16_f16 v[66:81], v[90:93], v[108:111], v[66:81]
	ds_read_b64 v[108:109], v123 offset:2192
	ds_read_b64 v[110:111], v123 offset:2200
	s_waitcnt lgkmcnt(2)
	v_mfma_f32_32x32x16_f16 v[66:81], v[94:97], v[124:127], v[66:81]
	s_waitcnt lgkmcnt(0)
	v_mfma_f32_32x32x16_f16 v[66:81], v[118:121], v[108:111], v[66:81]
	v_bfe_u32 v124, v99, 8, 8
	v_mul_lo_u16_e32 v126, 0x4f, v124
	v_lshrrev_b16_e32 v126, 9, v126
	v_and_b32_e32 v126, 62, v126
	v_add_u32_e32 v126, v124, v126
	v_mov_b32_e32 v123, s8
	v_mad_u32_u24 v126, v126, s6, v123
	v_mad_u32_u24 v123, v115, s6, v126
	v_mad_u32_u24 v102, v115, s12, v126
	ds_read_b64 v[108:109], v123 offset:32
	ds_read_b64 v[110:111], v123 offset:40
	ds_read_b64 v[124:125], v123 offset:1112
	ds_read_b64 v[126:127], v123 offset:1120
	v_add_f32_e32 v66, v107, v66
	v_add_f32_e32 v67, v107, v67
	v_add_f32_e32 v68, v107, v68
	v_add_f32_e32 v69, v107, v69
	v_add_f32_e32 v70, v112, v70
	v_add_f32_e32 v71, v112, v71
	v_add_f32_e32 v72, v112, v72
	v_add_f32_e32 v73, v112, v73
	v_add_f32_e32 v74, v113, v74
	v_add_f32_e32 v75, v113, v75
	v_add_f32_e32 v76, v113, v76
	v_add_f32_e32 v77, v113, v77
	v_add_f32_e32 v78, v117, v78
	v_add_f32_e32 v79, v117, v79
	v_add_f32_e32 v80, v117, v80
	v_add_f32_e32 v81, v117, v81
	v_cvt_pk_f16_f32 v66, v66, v67
	v_cvt_pk_f16_f32 v67, v68, v69
	v_cvt_pk_f16_f32 v68, v70, v71
	v_cvt_pk_f16_f32 v69, v72, v73
	v_cvt_pk_f16_f32 v70, v74, v75
	v_cvt_pk_f16_f32 v71, v76, v77
	v_cvt_pk_f16_f32 v72, v78, v79
	v_cvt_pk_f16_f32 v73, v80, v81
	v_pk_max_f16 v66, v66, 0
	v_pk_max_f16 v67, v67, 0
	v_pk_max_f16 v68, v68, 0
	v_pk_max_f16 v69, v69, 0
	v_pk_max_f16 v70, v70, 0
	v_pk_max_f16 v71, v71, 0
	v_pk_max_f16 v72, v72, 0
	v_pk_max_f16 v73, v73, 0
	ds_write2_b64 v101, v[66:67], v[68:69] offset1:6
	ds_write2_b64 v101, v[70:71], v[72:73] offset0:12 offset1:18
	v_bfe_u32 v101, v99, 8, 8
	v_mad_u32_u24 v122, v115, 24, s7
	v_mad_u32_u24 v101, v101, s13, v122
	s_waitcnt lgkmcnt(4)
	v_mfma_f32_32x32x16_f16 v[66:81], v[82:85], v[108:111], 0
	ds_read_b64 v[108:109], v123 offset:2264
	ds_read_b64 v[110:111], v123 offset:2272
	s_waitcnt lgkmcnt(2)
	v_mfma_f32_32x32x16_f16 v[66:81], v[86:89], v[124:127], v[66:81]
	ds_read_b64 v[124:125], v102 offset:176
	ds_read_b64 v[126:127], v102 offset:184
	s_waitcnt lgkmcnt(2)
	v_mfma_f32_32x32x16_f16 v[66:81], v[90:93], v[108:111], v[66:81]
	ds_read_b64 v[108:109], v123 offset:2192
	ds_read_b64 v[110:111], v123 offset:2200
	s_waitcnt lgkmcnt(2)
	v_mfma_f32_32x32x16_f16 v[66:81], v[94:97], v[124:127], v[66:81]
	s_waitcnt lgkmcnt(0)
	v_mfma_f32_32x32x16_f16 v[66:81], v[118:121], v[108:111], v[66:81]
	v_bfe_u32 v124, v99, 16, 8
	v_mul_lo_u16_e32 v126, 0x4f, v124
	v_lshrrev_b16_e32 v126, 9, v126
	v_and_b32_e32 v126, 62, v126
	v_add_u32_e32 v126, v124, v126
	v_mov_b32_e32 v123, s8
	v_mad_u32_u24 v126, v126, s6, v123
	v_mad_u32_u24 v123, v115, s6, v126
	v_mad_u32_u24 v102, v115, s12, v126
	ds_read_b64 v[108:109], v123 offset:32
	ds_read_b64 v[110:111], v123 offset:40
	ds_read_b64 v[124:125], v123 offset:1112
	ds_read_b64 v[126:127], v123 offset:1120
	v_add_f32_e32 v66, v107, v66
	v_add_f32_e32 v67, v107, v67
	v_add_f32_e32 v68, v107, v68
	v_add_f32_e32 v69, v107, v69
	v_add_f32_e32 v70, v112, v70
	v_add_f32_e32 v71, v112, v71
	v_add_f32_e32 v72, v112, v72
	v_add_f32_e32 v73, v112, v73
	v_add_f32_e32 v74, v113, v74
	v_add_f32_e32 v75, v113, v75
	v_add_f32_e32 v76, v113, v76
	v_add_f32_e32 v77, v113, v77
	v_add_f32_e32 v78, v117, v78
	v_add_f32_e32 v79, v117, v79
	v_add_f32_e32 v80, v117, v80
	v_add_f32_e32 v81, v117, v81
	v_cvt_pk_f16_f32 v66, v66, v67
	v_cvt_pk_f16_f32 v67, v68, v69
	v_cvt_pk_f16_f32 v68, v70, v71
	v_cvt_pk_f16_f32 v69, v72, v73
	v_cvt_pk_f16_f32 v70, v74, v75
	v_cvt_pk_f16_f32 v71, v76, v77
	v_cvt_pk_f16_f32 v72, v78, v79
	v_cvt_pk_f16_f32 v73, v80, v81
	v_pk_max_f16 v66, v66, 0
	v_pk_max_f16 v67, v67, 0
	v_pk_max_f16 v68, v68, 0
	v_pk_max_f16 v69, v69, 0
	v_pk_max_f16 v70, v70, 0
	v_pk_max_f16 v71, v71, 0
	v_pk_max_f16 v72, v72, 0
	v_pk_max_f16 v73, v73, 0
	ds_write2_b64 v101, v[66:67], v[68:69] offset1:6
	ds_write2_b64 v101, v[70:71], v[72:73] offset0:12 offset1:18
	v_bfe_u32 v101, v99, 16, 8
	v_mad_u32_u24 v122, v115, 24, s7
	v_mad_u32_u24 v101, v101, s13, v122
	s_waitcnt lgkmcnt(4)
	v_mfma_f32_32x32x16_f16 v[66:81], v[82:85], v[108:111], 0
	ds_read_b64 v[108:109], v123 offset:2264
	ds_read_b64 v[110:111], v123 offset:2272
	s_waitcnt lgkmcnt(2)
	v_mfma_f32_32x32x16_f16 v[66:81], v[86:89], v[124:127], v[66:81]
	ds_read_b64 v[124:125], v102 offset:176
	ds_read_b64 v[126:127], v102 offset:184
	s_waitcnt lgkmcnt(2)
	v_mfma_f32_32x32x16_f16 v[66:81], v[90:93], v[108:111], v[66:81]
	ds_read_b64 v[108:109], v123 offset:2192
	ds_read_b64 v[110:111], v123 offset:2200
	s_waitcnt lgkmcnt(2)
	v_mfma_f32_32x32x16_f16 v[66:81], v[94:97], v[124:127], v[66:81]
	s_waitcnt lgkmcnt(0)
	v_mfma_f32_32x32x16_f16 v[66:81], v[118:121], v[108:111], v[66:81]
	v_or_b32_e32 v99, 32, v114
	v_or_b32_e32 v102, 64, v114
	s_nop 9
	v_add_f32_e32 v66, v107, v66
	v_add_f32_e32 v67, v107, v67
	v_add_f32_e32 v68, v107, v68
	v_add_f32_e32 v69, v107, v69
	v_add_f32_e32 v70, v112, v70
	v_add_f32_e32 v71, v112, v71
	v_add_f32_e32 v72, v112, v72
	v_add_f32_e32 v73, v112, v73
	v_add_f32_e32 v74, v113, v74
	v_add_f32_e32 v75, v113, v75
	v_add_f32_e32 v76, v113, v76
	v_add_f32_e32 v77, v113, v77
	v_add_f32_e32 v78, v117, v78
	v_add_f32_e32 v79, v117, v79
	v_add_f32_e32 v80, v117, v80
	v_add_f32_e32 v81, v117, v81
	v_cvt_pk_f16_f32 v66, v66, v67
	v_cvt_pk_f16_f32 v67, v68, v69
	v_cvt_pk_f16_f32 v68, v70, v71
	v_cvt_pk_f16_f32 v69, v72, v73
	v_cvt_pk_f16_f32 v70, v74, v75
	v_cvt_pk_f16_f32 v71, v76, v77
	v_cvt_pk_f16_f32 v72, v78, v79
	v_cvt_pk_f16_f32 v73, v80, v81
	v_pk_max_f16 v66, v66, 0
	v_pk_max_f16 v67, v67, 0
	v_pk_max_f16 v68, v68, 0
	v_pk_max_f16 v69, v69, 0
	v_pk_max_f16 v70, v70, 0
	v_pk_max_f16 v71, v71, 0
	v_pk_max_f16 v72, v72, 0
	v_pk_max_f16 v73, v73, 0
	ds_write2_b64 v101, v[66:67], v[68:69] offset1:6
	ds_write2_b64 v101, v[70:71], v[72:73] offset0:12 offset1:18
	v_or_b32_e32 v101, 0x60, v114
